# v15 + static s_setprio 3 for the router task waves in both router phases (copy waves stay at 0)
# baseline (speedup 1.0000x reference)
; #define LAS __attribute__((address_space(3)))
; template <class T> __device__ __forceinline__ T* wsp(const Frame& F, size_t off) { return (T*)(F.ws + off); }
;     typedef float f4 __attribute__((ext_vector_type(4)));
;     const int gw = F.vcu * NWAVES + F.wave, NGW = F.G * NWAVES;
;     LAS float* lg = (LAS float*)(F.lds + RING_OFF + F.wave * 20480);
;     const bf16* TH = wsp<const bf16>(F, WS_HX); const bf16* TLo = wsp<const bf16>(F, WS_TOKLO);
;     const bf16* WH = wsp<const bf16>(F, WS_WRT) + (size_t)layer * 2 * 64 * 1024; const bf16* WL = WH + 64 * 1024;
;     const float* rbias = inp(F, I_RTB) + layer * 64;
;     unsigned* cnt = (unsigned*)(F.ctl + CW_CNT) + layer * NCH * 64 * CNT_STRIDE + cnt_off;
;     int* LIST = wsp<int>(F, WS_LIST); int* TS = wsp<int>(F, WS_TOKSLOT); float* TG = wsp<float>(F, WS_TOKGATE);
;     const int lr = F.lane & 15, lq = F.lane >> 4;
;     for (int task = F.wave * F.G + F.vcu; task < ntok / 64; task += NGW) {
.LBB0_654:
	s_cmp_lt_i32 s34, 7
	s_cselect_b64 s[0:1], -1, 0
	s_and_b64 s[2:3], s[0:1], s[4:5]
	s_andn2_b64 vcc, exec, s[2:3]
	s_cbranch_vccnz .LBB0_680
	v_mov_b32_e32 v2, v0
	s_add_i32 s2, 0, 0x20290
	v_mov_b32_e32 v1, s2
	ds_read_b64 v[4:5], v1
	v_readfirstlane_b32 s2, v2
	s_ashr_i32 s10, s2, 6
	s_mul_i32 s3, s10, s67
	s_add_i32 s9, s3, s71
	s_waitcnt lgkmcnt(0)
	v_readfirstlane_b32 s2, v4
	s_cmpk_gt_i32 s9, 0x21f
	v_readfirstlane_b32 s3, v5
	s_cbranch_scc1 .Lcv0_entry
	s_setprio 3
	v_mov_b32_e32 v197, 0
	v_and_b32_e32 v194, 48, v2
	v_mov_b32_e32 v195, v197
	v_and_b32_e32 v1, 63, v2
	v_and_b32_e32 v231, 15, v2
	v_bfe_u32 v4, v2, 4, 2
	v_lshl_add_u64 v[2:3], s[38:39], 0, v[194:195]
	s_mov_b64 s[16:17], 0x8800000
	v_lshl_add_u64 v[198:199], v[2:3], 0, s[16:17]
	s_mov_b64 s[16:17], 0x14c00000
	v_lshlrev_b32_e32 v196, 11, v231
	v_lshl_add_u64 v[200:201], v[2:3], 0, s[16:17]
	v_lshl_add_u64 v[2:3], s[38:39], 0, v[196:197]
	v_lshl_add_u64 v[2:3], v[2:3], 0, v[194:195]
	s_mov_b64 s[16:17], 0x1400000
	v_lshl_add_u64 v[202:203], v[2:3], 0, s[16:17]
	s_mov_b64 s[16:17], 0x1420000
	s_lshl_b32 s22, s67, 3
	v_lshl_add_u64 v[204:205], v[2:3], 0, s[16:17]
	s_mov_b64 s[16:17], 0x1408000
	s_add_u32 s4, s36, 0x10000
	s_mulk_i32 s10, 0x5000
	v_lshl_add_u64 v[206:207], v[2:3], 0, s[16:17]
	s_mov_b64 s[16:17], 0x1428000
	s_addc_u32 s5, s37, 0
	s_add_i32 s23, s10, 0
	v_lshl_add_u64 v[208:209], v[2:3], 0, s[16:17]
	s_mov_b64 s[16:17], 0x1410000
	s_add_u32 s10, s38, 0x1ec0000
	v_lshl_add_u64 v[210:211], v[2:3], 0, s[16:17]
	s_mov_b64 s[16:17], 0x1430000
	s_addc_u32 s11, s39, 0
	v_lshl_add_u64 v[212:213], v[2:3], 0, s[16:17]
	s_mov_b64 s[16:17], 0x1418000
	s_add_u32 s12, s38, 0x1d80000
	v_lshl_add_u64 v[214:215], v[2:3], 0, s[16:17]
	s_mov_b64 s[16:17], 0x1438000
	s_addc_u32 s13, s39, 0
	v_lshlrev_b32_e32 v5, 2, v231
	v_lshl_add_u64 v[216:217], v[2:3], 0, s[16:17]
	v_mul_u32_u24_e32 v2, 0x410, v4
	s_add_u32 s14, s38, 0x1500000
	v_add3_u32 v195, s23, v5, v2
	s_movk_i32 s16, 0x104
	v_mov_b32_e32 v2, s23
	v_or_b32_e32 v196, v196, v194
	s_addc_u32 s15, s39, 0
	v_mad_u32_u24 v232, v1, s16, v2
	v_lshl_add_u32 v233, v1, 2, s23
	v_lshlrev_b32_e32 v234, 6, v1
	v_mov_b64_e32 v[218:219], v[196:197]
	v_lshl_or_b32 v220, s9, 6, v231
	s_lshl_b32 s40, s67, 9
	s_mov_b32 s41, 0x8000
	s_mov_b32 s42, 0x10000
	s_mov_b32 s43, 0x18000
	s_mov_b32 s44, 0x8800000
	s_mov_b32 s45, 0x14c00000
	s_mov_b32 s46, 0x8808000
	s_mov_b32 s47, 0x14c08000
	s_mov_b32 s48, 0x8810000
	s_mov_b32 s49, 0x14c10000
	s_mov_b32 s50, 0x8818000
	s_mov_b32 s51, 0x14c18000
	s_mov_b32 s52, 0x1400000
	s_mov_b32 s53, 0x1420000
	s_mov_b32 s54, 0x1408000
	s_mov_b32 s55, 0x1428000
	s_mov_b32 s56, 0x1410000
	s_mov_b32 s57, 0x1430000
	s_mov_b32 s58, 0x1418000
	s_mov_b32 s59, 0x1438000
	s_mov_b64 s[16:17], 0x80
	v_mov_b32_e32 v235, 1
	s_mov_b32 s60, 0x40200000
	s_mov_b32 s61, 0x22000
	v_mov_b32_e32 v236, 0xff800000
	s_branch .LBB0_658

;     __device__ __forceinline__ void st(const void* p, const u32x4& v) const { __builtin_amdgcn_raw_buffer_store_b128(v, r, (unsigned)((const unsigned char*)p - b), 0, EPI_SC1); }
; __device__ __forceinline__ unsigned xb_ld(unsigned* p)              { return __hip_atomic_load(p, __ATOMIC_RELAXED, __HIP_MEMORY_SCOPE_AGENT); }
; __device__ __forceinline__ void xcd_barrier_complete(unsigned* bar, unsigned x, unsigned& nloc, unsigned& nx) {
;     const unsigned G = gridDim.x * gridDim.y * gridDim.z;
;     unsigned sum, cnt, mine, sp = 0u;
;     for (;;) {
;         sum = 0u; cnt = 0u; mine = 0u;
; #pragma unroll
;         for (unsigned j = 0; j < 16; ++j) { const unsigned c = xb_ld(&bar[XB_XCNT(j)]); sum += c; cnt += (c > 0u) ? 1u : 0u; mine = (j == x) ? c : mine; }
; __device__ __forceinline__ void xcd_barrier(const XcdBarrier& b) {
;     asm volatile("s_waitcnt vmcnt(0)" ::: "memory");
;     __syncthreads();
;     if (threadIdx.x == 0) {
;         unsigned* bar = b.bar;
;         __builtin_amdgcn_s_waitcnt(0);
;         unsigned nloc = b.st[0], nx = b.st[1];
;         if (nloc == 0u) { xcd_barrier_complete(bar, b.x, nloc, nx); b.st[0] = nloc; b.st[1] = nx; }
.Lcv0_end:
.LBB0_680:
	s_setprio 0
	s_cmp_gt_i32 s35, 7
	s_cselect_b64 s[2:3], -1, 0
	s_and_b64 s[0:1], s[0:1], s[2:3]
	s_andn2_b64 vcc, exec, s[0:1]
	s_cbranch_vccnz .LBB0_734
	s_waitcnt vmcnt(0)
	s_waitcnt vmcnt(0) lgkmcnt(0)
	s_barrier
	s_and_saveexec_b64 s[0:1], s[6:7]
	s_cbranch_execz .LBB0_733
	s_add_i32 s4, 0, 0x20160
	v_mov_b32_e32 v1, s4
	s_waitcnt vmcnt(0) expcnt(0) lgkmcnt(0)
	ds_read_b32 v3, v1
	s_add_i32 s4, 0, 0x20164
	v_mov_b32_e32 v1, s4
	ds_read_b32 v1, v1
	s_waitcnt lgkmcnt(1)
	v_cmp_ne_u32_e32 vcc, 0, v3
	s_cbranch_vccnz .LBB0_697
	s_load_dwordx2 s[12:13], s[92:93], 0x4
	s_add_u32 s4, s26, 0x4200
	s_addc_u32 s5, s27, 0
	s_add_u32 s10, s26, 0x4400
	s_addc_u32 s11, s27, 0
	s_waitcnt lgkmcnt(0)
	s_mul_i32 s9, s12, s67
	s_add_u32 s12, s26, 0x4500
	s_mul_i32 s9, s9, s13
	s_addc_u32 s13, s27, 0
	s_add_u32 s14, s26, 0x4600
	s_addc_u32 s15, s27, 0
	s_add_u32 s16, s26, 0x4700
	s_addc_u32 s17, s27, 0
	s_add_u32 s18, s26, 0x4800
	s_addc_u32 s19, s27, 0
	s_add_u32 s20, s26, 0x4900
	s_addc_u32 s21, s27, 0
	s_add_u32 s22, s26, 0x4a00
	s_addc_u32 s23, s27, 0
	s_add_u32 s40, s26, 0x4b00
	s_addc_u32 s41, s27, 0
	s_add_u32 s42, s26, 0x4c00
	s_addc_u32 s43, s27, 0
	s_add_u32 s44, s26, 0x4d00
	s_addc_u32 s45, s27, 0
	s_add_u32 s46, s26, 0x4e00
	s_addc_u32 s47, s27, 0
	s_add_u32 s48, s26, 0x4f00
	s_addc_u32 s49, s27, 0
	s_add_u32 s50, s26, 0x5000
	s_addc_u32 s51, s27, 0
	s_add_u32 s52, s26, 0x5100
	s_addc_u32 s53, s27, 0
	s_add_u32 s54, s26, 0x5200
	s_addc_u32 s55, s27, 0
	s_add_u32 s56, s26, 0x5300
	s_addc_u32 s57, s27, 0
	s_mov_b32 s64, 1
	v_mov_b32_e32 v17, 0
	s_branch .LBB0_685

; #define LAS __attribute__((address_space(3)))
; template <class T> __device__ __forceinline__ T* wsp(const Frame& F, size_t off) { return (T*)(F.ws + off); }
;     typedef float f4 __attribute__((ext_vector_type(4)));
;     const int gw = F.vcu * NWAVES + F.wave, NGW = F.G * NWAVES;
;     LAS float* lg = (LAS float*)(F.lds + RING_OFF + F.wave * 20480);
;     const bf16* TH = wsp<const bf16>(F, WS_HX); const bf16* TLo = wsp<const bf16>(F, WS_TOKLO);
;     const bf16* WH = wsp<const bf16>(F, WS_WRT) + (size_t)layer * 2 * 64 * 1024; const bf16* WL = WH + 64 * 1024;
;     const float* rbias = inp(F, I_RTB) + layer * 64;
;     unsigned* cnt = (unsigned*)(F.ctl + CW_CNT) + layer * NCH * 64 * CNT_STRIDE + cnt_off;
;     int* LIST = wsp<int>(F, WS_LIST); int* TS = wsp<int>(F, WS_TOKSLOT); float* TG = wsp<float>(F, WS_TOKGATE);
;     const int lr = F.lane & 15, lq = F.lane >> 4;
;     for (int task = F.wave * F.G + F.vcu; task < ntok / 64; task += NGW) {
.LBB0_1506:
	s_cmp_lt_i32 s34, 16
	s_cselect_b64 s[0:1], -1, 0
	s_and_b64 s[2:3], s[0:1], s[4:5]
	s_andn2_b64 vcc, exec, s[2:3]
	s_cbranch_vccnz .LBB0_1532
	v_mov_b32_e32 v2, v0
	s_add_i32 s2, 0, 0x20290
	v_mov_b32_e32 v1, s2
	s_waitcnt lgkmcnt(0)
	ds_read_b64 v[4:5], v1
	v_readfirstlane_b32 s2, v2
	s_ashr_i32 s8, s2, 6
	s_mul_i32 s3, s8, s67
	s_add_i32 s20, s3, s71
	s_waitcnt lgkmcnt(0)
	v_readfirstlane_b32 s2, v4
	s_cmpk_gt_i32 s20, 0x1ff
	v_readfirstlane_b32 s3, v5
	s_cbranch_scc1 .Lcv1_entry
	s_setprio 3
	v_mov_b32_e32 v197, 0
	v_and_b32_e32 v194, 48, v2
	v_mov_b32_e32 v195, v197
	v_and_b32_e32 v1, 63, v2
	v_and_b32_e32 v231, 15, v2
	v_bfe_u32 v4, v2, 4, 2
	v_lshl_add_u64 v[2:3], s[38:39], 0, v[194:195]
	s_mov_b64 s[14:15], 0x8800000
	v_lshl_add_u64 v[198:199], v[2:3], 0, s[14:15]
	s_mov_b64 s[14:15], 0x14c00000
	v_lshlrev_b32_e32 v196, 11, v231
	v_lshl_add_u64 v[200:201], v[2:3], 0, s[14:15]
	v_lshl_add_u64 v[2:3], s[38:39], 0, v[196:197]
	v_lshl_add_u64 v[2:3], v[2:3], 0, v[194:195]
	s_mov_b64 s[14:15], 0x1440000
	v_lshl_add_u64 v[202:203], v[2:3], 0, s[14:15]
	s_mov_b64 s[14:15], 0x1460000
	s_lshl_b32 s21, s67, 3
	v_lshl_add_u64 v[204:205], v[2:3], 0, s[14:15]
	s_mov_b64 s[14:15], 0x1448000
	s_add_u32 s4, s36, 0x14000
	s_mulk_i32 s8, 0x5000
	v_lshl_add_u64 v[206:207], v[2:3], 0, s[14:15]
	s_mov_b64 s[14:15], 0x1468000
	s_addc_u32 s5, s37, 0
	s_add_i32 s22, s8, 0
	v_lshl_add_u64 v[208:209], v[2:3], 0, s[14:15]
	s_mov_b64 s[14:15], 0x1450000
	s_add_u32 s8, s38, 0x1ec0000
	v_lshl_add_u64 v[210:211], v[2:3], 0, s[14:15]
	s_mov_b64 s[14:15], 0x1470000
	s_addc_u32 s9, s39, 0
	v_lshl_add_u64 v[212:213], v[2:3], 0, s[14:15]
	s_mov_b64 s[14:15], 0x1458000
	s_add_u32 s10, s38, 0x1d80000
	v_lshl_add_u64 v[214:215], v[2:3], 0, s[14:15]
	s_mov_b64 s[14:15], 0x1478000
	s_addc_u32 s11, s39, 0
	v_lshlrev_b32_e32 v5, 2, v231
	v_lshl_add_u64 v[216:217], v[2:3], 0, s[14:15]
	v_mul_u32_u24_e32 v2, 0x410, v4
	s_add_u32 s12, s38, 0x1500000
	v_add3_u32 v195, s22, v5, v2
	s_movk_i32 s14, 0x104
	v_mov_b32_e32 v2, s22
	v_or_b32_e32 v196, v196, v194
	s_addc_u32 s13, s39, 0
	v_mad_u32_u24 v232, v1, s14, v2
	v_lshl_add_u32 v233, v1, 2, s22
	v_lshlrev_b32_e32 v234, 6, v1
	v_mov_b64_e32 v[218:219], v[196:197]
	v_lshl_or_b32 v220, s20, 6, v231
	s_lshl_b32 s23, s67, 9
	s_mov_b32 s40, 0x8000
	s_mov_b32 s41, 0x10000
	s_mov_b32 s42, 0x18000
	s_mov_b32 s43, 0x8800000
	s_mov_b32 s44, 0x14c00000
	s_mov_b32 s45, 0x8808000
	s_mov_b32 s46, 0x14c08000
	s_mov_b32 s47, 0x8810000
	s_mov_b32 s48, 0x14c10000
	s_mov_b32 s49, 0x8818000
	s_mov_b32 s50, 0x14c18000
	s_mov_b32 s51, 0x1440000
	s_mov_b32 s52, 0x1460000
	s_mov_b32 s53, 0x1448000
	s_mov_b32 s54, 0x1468000
	s_mov_b32 s55, 0x1450000
	s_mov_b32 s56, 0x1470000
	s_mov_b32 s57, 0x1458000
	s_mov_b32 s58, 0x1478000
	s_mov_b64 s[14:15], 0x80
	v_mov_b32_e32 v235, 1
	s_mov_b32 s59, 0x40200000
	s_mov_b32 s60, 0x22000
	v_mov_b32_e32 v236, 0xff800000
	s_branch .LBB0_1510

;     __device__ __forceinline__ void st(const void* p, const u32x4& v) const { __builtin_amdgcn_raw_buffer_store_b128(v, r, (unsigned)((const unsigned char*)p - b), 0, EPI_SC1); }
; __device__ __forceinline__ unsigned xb_ld(unsigned* p)              { return __hip_atomic_load(p, __ATOMIC_RELAXED, __HIP_MEMORY_SCOPE_AGENT); }
; __device__ __forceinline__ void xcd_barrier_complete(unsigned* bar, unsigned x, unsigned& nloc, unsigned& nx) {
;     const unsigned G = gridDim.x * gridDim.y * gridDim.z;
;     unsigned sum, cnt, mine, sp = 0u;
;     for (;;) {
;         sum = 0u; cnt = 0u; mine = 0u;
; #pragma unroll
;         for (unsigned j = 0; j < 16; ++j) { const unsigned c = xb_ld(&bar[XB_XCNT(j)]); sum += c; cnt += (c > 0u) ? 1u : 0u; mine = (j == x) ? c : mine; }
; __device__ __forceinline__ void xcd_barrier(const XcdBarrier& b) {
;     asm volatile("s_waitcnt vmcnt(0)" ::: "memory");
;     __syncthreads();
;     if (threadIdx.x == 0) {
;         unsigned* bar = b.bar;
;         __builtin_amdgcn_s_waitcnt(0);
;         unsigned nloc = b.st[0], nx = b.st[1];
;         if (nloc == 0u) { xcd_barrier_complete(bar, b.x, nloc, nx); b.st[0] = nloc; b.st[1] = nx; }
.Lcv1_end:
.LBB0_1532:
	s_setprio 0
	s_cmp_gt_i32 s35, 16
	s_cselect_b64 s[2:3], -1, 0
	s_and_b64 s[0:1], s[0:1], s[2:3]
	s_andn2_b64 vcc, exec, s[0:1]
	s_cbranch_vccnz .LBB0_1586
	s_waitcnt vmcnt(0)
	s_waitcnt vmcnt(0) lgkmcnt(0)
	s_barrier
	s_and_saveexec_b64 s[0:1], s[6:7]
	s_cbranch_execz .LBB0_1585
	s_add_i32 s4, 0, 0x20160
	v_mov_b32_e32 v1, s4
	s_waitcnt vmcnt(0) expcnt(0) lgkmcnt(0)
	ds_read_b32 v3, v1
	s_add_i32 s4, 0, 0x20164
	v_mov_b32_e32 v1, s4
	ds_read_b32 v1, v1
	s_waitcnt lgkmcnt(1)
	v_cmp_ne_u32_e32 vcc, 0, v3
	s_cbranch_vccnz .LBB0_1549
	s_load_dwordx2 s[10:11], s[92:93], 0x4
	s_add_u32 s4, s26, 0x4200
	s_addc_u32 s5, s27, 0
	s_add_u32 s8, s26, 0x4400
	s_addc_u32 s9, s27, 0
	s_waitcnt lgkmcnt(0)
	s_mul_i32 s62, s10, s67
	s_add_u32 s10, s26, 0x4500
	s_mul_i32 s62, s62, s11
	s_addc_u32 s11, s27, 0
	s_add_u32 s12, s26, 0x4600
	s_addc_u32 s13, s27, 0
	s_add_u32 s14, s26, 0x4700
	s_addc_u32 s15, s27, 0
	s_add_u32 s16, s26, 0x4800
	s_addc_u32 s17, s27, 0
	s_add_u32 s18, s26, 0x4900
	s_addc_u32 s19, s27, 0
	s_add_u32 s20, s26, 0x4a00
	s_addc_u32 s21, s27, 0
	s_add_u32 s22, s26, 0x4b00
	s_addc_u32 s23, s27, 0
	s_add_u32 s40, s26, 0x4c00
	s_addc_u32 s41, s27, 0
	s_add_u32 s42, s26, 0x4d00
	s_addc_u32 s43, s27, 0
	s_add_u32 s44, s26, 0x4e00
	s_addc_u32 s45, s27, 0
	s_add_u32 s46, s26, 0x4f00
	s_addc_u32 s47, s27, 0
	s_add_u32 s48, s26, 0x5000
	s_addc_u32 s49, s27, 0
	s_add_u32 s50, s26, 0x5100
	s_addc_u32 s51, s27, 0
	s_add_u32 s52, s26, 0x5200
	s_addc_u32 s53, s27, 0
	s_add_u32 s54, s26, 0x5300
	s_addc_u32 s55, s27, 0
	s_mov_b32 s63, 1
	v_mov_b32_e32 v17, 0
	s_branch .LBB0_1537
